# second poll bank delayed by s_sleep 2 (fine-tune of the bank offset, v60 uses 3)
# speedup vs baseline: 1.0270x; 1.0080x over previous
.Lr0_rdy:
	v_lshl_add_u32 v66, s54, 11, v1
	ds_read_b128 a[0:3], v66
	ds_read_b128 a[4:7], v66 offset:1024
	s_cmp_eq_u32 s54, 0
	s_cbranch_scc1 .Lr0_first
	s_sleep 2
	global_load_dwordx4 v[164:167], v[196:197], off nt
	global_load_dwordx4 v[168:171], v[196:197], off offset:1024 nt
	global_load_dwordx4 v[172:175], v[196:197], off offset:2048 nt
	global_load_dwordx4 v[176:179], v[196:197], off offset:3072 nt
	global_load_dwordx4 v[180:183], v[198:199], off nt
	global_load_dwordx4 v[184:187], v[198:199], off offset:1024 nt
	global_load_dwordx4 v[188:191], v[198:199], off offset:2048 nt
	global_load_dwordx4 v[192:195], v[198:199], off offset:3072 nt
	s_mov_b32 s55, 0
	s_waitcnt lgkmcnt(0)
